# stack12 + 48 B of unreachable padding after the strip loop: all downstream code back at its stack10 placement modulo 64 B
# speedup vs baseline: 1.0038x; 1.0026x over previous
; #define GAS __attribute__((address_space(1)))
; #define LAS __attribute__((address_space(3)))
; __device__ __forceinline__ float hlo(unsigned w) { return (float)__builtin_bit_cast(f16x2_t_, w)[0]; }
; __device__ __forceinline__ float hhi(unsigned w) { return (float)__builtin_bit_cast(f16x2_t_, w)[1]; }
; __device__ __forceinline__ unsigned q4c(f32x4 v, float q) {
;     v = v * q; v.x = __builtin_fminf(__builtin_fmaxf(v.x, -127.f), 127.f); v.y = __builtin_fminf(__builtin_fmaxf(v.y, -127.f), 127.f); v.z = __builtin_fminf(__builtin_fmaxf(v.z, -127.f), 127.f); v.w = __builtin_fminf(__builtin_fmaxf(v.w, -127.f), 127.f);
;     return q4(v, 1.0f); }
; __device__ __forceinline__ void strip_quant(LAS unsigned char* lds, unsigned char* dst, float* cmout, int wave, int lane) {
; #pragma unroll
;     for (int rr = 0; rr < 4; ++rr) { const int n = 4 * wave + rr; const LAS v4u* s = (const LAS v4u*)(lds + n * SROW) + lane;
;         v4u w[4]; float mx = 0.f;
; #pragma unroll
;         for (int j = 0; j < 4; ++j) { w[j] = s[64 * j];
;             mx = __builtin_fmaxf(mx, __builtin_fmaxf(__builtin_fmaxf(__builtin_fmaxf(__builtin_fabsf(hlo(w[j].x)), __builtin_fabsf(hhi(w[j].x))), __builtin_fmaxf(__builtin_fabsf(hlo(w[j].y)), __builtin_fabsf(hhi(w[j].y)))),
;                                                  __builtin_fmaxf(__builtin_fmaxf(__builtin_fabsf(hlo(w[j].z)), __builtin_fabsf(hhi(w[j].z))), __builtin_fmaxf(__builtin_fabsf(hlo(w[j].w)), __builtin_fabsf(hhi(w[j].w)))))); }
;         mx = wave_max(mx); const float q = 127.0f / __builtin_fmaxf(mx, 1e-30f);
;         GAS v2u* d = (GAS v2u*)(dst + (size_t)n * DM) + lane;
; #pragma unroll
;         for (int j = 0; j < 4; ++j) { v2u o; o.x = q4c((f32x4){hlo(w[j].x), hhi(w[j].x), hlo(w[j].y), hhi(w[j].y)}, q); o.y = q4c((f32x4){hlo(w[j].z), hhi(w[j].z), hlo(w[j].w), hhi(w[j].w)}, q); __builtin_nontemporal_store(o, d + 64 * j); }
;         if (lane == 0) cmout[n] = mx; }
.LBB0_30:
	s_or_b64 exec, exec, s[12:13]
	v_add_u32_e32 v2, s15, v163
	ds_read_b128 v[14:17], v2
	ds_read_b128 v[10:13], v2 offset:1024
	s_waitcnt lgkmcnt(1)
	v_max_f16_e64 v3, |v14|, |v14|
	v_max_f16_sdwa v4, |v14|, |v14| dst_sel:DWORD dst_unused:UNUSED_PAD src0_sel:WORD_1 src1_sel:WORD_1
	v_max_f16_e32 v3, v3, v4
	v_max_f16_e64 v4, |v15|, |v15|
	v_max_f16_sdwa v5, |v15|, |v15| dst_sel:DWORD dst_unused:UNUSED_PAD src0_sel:WORD_1 src1_sel:WORD_1
	v_max_f16_e32 v4, v4, v5
	v_max_f16_e64 v5, |v17|, |v17|
	v_max_f16_sdwa v6, |v17|, |v17| dst_sel:DWORD dst_unused:UNUSED_PAD src0_sel:WORD_1 src1_sel:WORD_1
	v_lshrrev_b32_e32 v167, 16, v16
	v_max_f16_e32 v5, v5, v6
	v_max3_f16 v5, |v16|, |v167|, v5
	v_max3_f16 v3, v3, v4, v5
	s_waitcnt lgkmcnt(0)
	v_max_f16_e64 v4, |v10|, |v10|
	v_max_f16_sdwa v5, |v10|, |v10| dst_sel:DWORD dst_unused:UNUSED_PAD src0_sel:WORD_1 src1_sel:WORD_1
	v_max_f16_e32 v4, v4, v5
	v_max_f16_e64 v5, |v11|, |v11|
	v_max_f16_sdwa v6, |v11|, |v11| dst_sel:DWORD dst_unused:UNUSED_PAD src0_sel:WORD_1 src1_sel:WORD_1
	v_max_f16_e32 v5, v5, v6
	v_max_f16_e64 v6, |v13|, |v13|
	v_max_f16_sdwa v7, |v13|, |v13| dst_sel:DWORD dst_unused:UNUSED_PAD src0_sel:WORD_1 src1_sel:WORD_1
	v_lshrrev_b32_e32 v170, 16, v12
	v_max_f16_e32 v6, v6, v7
	v_max3_f16 v6, |v12|, |v170|, v6
	v_max3_f16 v4, v4, v5, v6
	ds_read_b128 v[6:9], v2 offset:2048
	v_cvt_f32_f16_e32 v3, v3
	v_cvt_f32_f16_e32 v4, v4
	s_waitcnt lgkmcnt(0)
	v_max_f16_sdwa v5, |v7|, |v7| dst_sel:DWORD dst_unused:UNUSED_PAD src0_sel:WORD_1 src1_sel:WORD_1
	v_max3_f32 v154, v3, 0, v4
	v_max_f16_e64 v3, |v6|, |v6|
	v_max_f16_sdwa v4, |v6|, |v6| dst_sel:DWORD dst_unused:UNUSED_PAD src0_sel:WORD_1 src1_sel:WORD_1
	v_max_f16_e32 v3, v3, v4
	v_max_f16_e64 v4, |v7|, |v7|
	v_max_f16_e32 v4, v4, v5
	v_max_f16_e64 v5, |v9|, |v9|
	v_max_f16_sdwa v166, |v9|, |v9| dst_sel:DWORD dst_unused:UNUSED_PAD src0_sel:WORD_1 src1_sel:WORD_1
	v_lshrrev_b32_e32 v171, 16, v8
	v_max_f16_e32 v5, v5, v166
	v_max3_f16 v5, |v8|, |v171|, v5
	v_max3_f16 v3, v3, v4, v5
	v_cvt_f32_f16_e32 v166, v3
	ds_read_b128 v[2:5], v2 offset:3072
	s_waitcnt lgkmcnt(0)
	v_max_f16_e64 v168, |v2|, |v2|
	v_max_f16_sdwa v169, |v2|, |v2| dst_sel:DWORD dst_unused:UNUSED_PAD src0_sel:WORD_1 src1_sel:WORD_1
	v_max_f16_e32 v168, v168, v169
	v_max_f16_e64 v169, |v3|, |v3|
	v_max_f16_sdwa v172, |v3|, |v3| dst_sel:DWORD dst_unused:UNUSED_PAD src0_sel:WORD_1 src1_sel:WORD_1
	v_max_f16_e64 v173, |v5|, |v5|
	v_max_f16_sdwa v174, |v5|, |v5| dst_sel:DWORD dst_unused:UNUSED_PAD src0_sel:WORD_1 src1_sel:WORD_1
	v_max_f16_e32 v169, v169, v172
	v_lshrrev_b32_e32 v172, 16, v4
	v_max_f16_e32 v173, v173, v174
	v_max3_f16 v173, |v4|, |v172|, v173
	v_max3_f16 v168, v168, v169, v173
	v_cvt_f32_f16_e32 v168, v168
	v_max3_f32 v154, v154, v166, v168
	ds_bpermute_b32 v166, v1, v154
	s_waitcnt lgkmcnt(0)
	v_max_f32_e32 v166, v166, v166
	v_max_f32_e32 v154, v154, v166
	ds_bpermute_b32 v166, v19, v154
	s_waitcnt lgkmcnt(0)
	v_max_f32_e32 v166, v166, v166
	v_max_f32_e32 v154, v154, v166
	ds_bpermute_b32 v166, v21, v154
	s_waitcnt lgkmcnt(0)
	v_max_f32_e32 v166, v166, v166
	v_max_f32_e32 v154, v154, v166
	ds_bpermute_b32 v166, v155, v154
	s_waitcnt lgkmcnt(0)
	v_max_f32_e32 v166, v166, v166
	v_max_f32_e32 v154, v154, v166
	ds_bpermute_b32 v166, v156, v154
	s_waitcnt lgkmcnt(0)
	v_max_f32_e32 v166, v166, v166
	v_max_f32_e32 v154, v154, v166
	ds_bpermute_b32 v166, v157, v154
	s_waitcnt lgkmcnt(0)
	v_max_f32_e32 v166, v166, v166
	v_max_f32_e32 v166, v154, v166
	v_max_f32_e32 v154, 0xda24260, v166
	v_div_scale_f32 v168, s[12:13], v154, v154, s50
	v_rcp_f32_e32 v169, v168
	s_add_u32 s12, s30, s24
	s_addc_u32 s13, s31, s25
	v_fma_f32 v173, -v168, v169, 1.0
	v_fmac_f32_e32 v169, v173, v169
	v_div_scale_f32 v173, vcc, s50, v154, s50
	v_mul_f32_e32 v174, v173, v169
	v_fma_f32 v175, -v168, v174, v173
	v_fmac_f32_e32 v174, v175, v169
	v_fma_f32 v168, -v168, v174, v173
	v_div_fmas_f32 v168, v168, v169, v174
	v_div_fixup_f32 v154, v168, v154, s50
	v_cvt_f32_f16_e32 v168, v14
	v_cvt_f32_f16_sdwa v169, v14 dst_sel:DWORD dst_unused:UNUSED_PAD src0_sel:WORD_1
	v_cvt_f32_f16_e32 v14, v15
	v_cvt_f32_f16_sdwa v15, v15 dst_sel:DWORD dst_unused:UNUSED_PAD src0_sel:WORD_1
	v_pk_mul_f32 v[168:169], v[168:169], v[154:155] op_sel_hi:[1,0]
	s_nop 0
	v_med3_f32 v169, v169, s51, v164
	v_pk_mul_f32 v[14:15], v[14:15], v[154:155] op_sel_hi:[1,0]
	v_med3_f32 v168, v168, s51, v164
	v_med3_f32 v14, v14, s51, v164
	v_med3_f32 v15, v15, s51, v164
	v_rndne_f32_e32 v169, v169
	v_rndne_f32_e32 v168, v168
	v_cvt_i32_f32_e32 v169, v169
	v_rndne_f32_e32 v14, v14
	v_rndne_f32_e32 v15, v15
	v_cvt_i32_f32_e32 v168, v168
	v_cvt_i32_f32_sdwa v14, v14 dst_sel:WORD_1 dst_unused:UNUSED_PAD src0_sel:DWORD
	v_cvt_i32_f32_e32 v15, v15
	v_lshlrev_b32_e32 v169, 8, v169
	v_and_b32_e32 v169, 0xff00, v169
	v_and_b32_e32 v14, 0xff0000, v14
	v_perm_b32 v15, v15, v168, s52
	v_or3_b32 v14, v15, v169, v14
	v_cvt_f32_f16_e32 v168, v16
	v_cvt_f32_f16_e32 v169, v167
	v_cvt_f32_f16_e32 v16, v17
	v_cvt_f32_f16_sdwa v17, v17 dst_sel:DWORD dst_unused:UNUSED_PAD src0_sel:WORD_1
	v_pk_mul_f32 v[168:169], v[168:169], v[154:155] op_sel_hi:[1,0]
	s_nop 0
	v_med3_f32 v167, v169, s51, v164
	v_pk_mul_f32 v[16:17], v[16:17], v[154:155] op_sel_hi:[1,0]
	v_med3_f32 v15, v168, s51, v164
	v_med3_f32 v16, v16, s51, v164
	v_med3_f32 v17, v17, s51, v164
	v_rndne_f32_e32 v167, v167
	v_rndne_f32_e32 v15, v15
	v_cvt_i32_f32_e32 v167, v167
	v_rndne_f32_e32 v16, v16
	v_rndne_f32_e32 v17, v17
	v_cvt_i32_f32_e32 v15, v15
	v_cvt_i32_f32_sdwa v16, v16 dst_sel:WORD_1 dst_unused:UNUSED_PAD src0_sel:DWORD
	v_cvt_i32_f32_e32 v17, v17
	v_lshlrev_b32_e32 v167, 8, v167
; #define GAS __attribute__((address_space(1)))
; __device__ __forceinline__ float hlo(unsigned w) { return (float)__builtin_bit_cast(f16x2_t_, w)[0]; }
; __device__ __forceinline__ float hhi(unsigned w) { return (float)__builtin_bit_cast(f16x2_t_, w)[1]; }
; __device__ __forceinline__ unsigned q4c(f32x4 v, float q) {
;     v = v * q; v.x = __builtin_fminf(__builtin_fmaxf(v.x, -127.f), 127.f); v.y = __builtin_fminf(__builtin_fmaxf(v.y, -127.f), 127.f); v.z = __builtin_fminf(__builtin_fmaxf(v.z, -127.f), 127.f); v.w = __builtin_fminf(__builtin_fmaxf(v.w, -127.f), 127.f);
;     return q4(v, 1.0f); }
; __device__ __forceinline__ void strip_quant(LAS unsigned char* lds, unsigned char* dst, float* cmout, int wave, int lane) {
;     ...
;         GAS v2u* d = (GAS v2u*)(dst + (size_t)n * DM) + lane;
; #pragma unroll
;         for (int j = 0; j < 4; ++j) { v2u o; o.x = q4c((f32x4){hlo(w[j].x), hhi(w[j].x), hlo(w[j].y), hhi(w[j].y)}, q); o.y = q4c((f32x4){hlo(w[j].z), hhi(w[j].z), hlo(w[j].w), hhi(w[j].w)}, q); __builtin_nontemporal_store(o, d + 64 * j); }
;         if (lane == 0) cmout[n] = mx; }
	v_and_b32_e32 v167, 0xff00, v167
	v_and_b32_e32 v16, 0xff0000, v16
	v_perm_b32 v15, v17, v15, s52
	v_or3_b32 v15, v15, v167, v16
	global_store_dwordx2 v165, v[14:15], s[12:13] nt
	v_cvt_f32_f16_e32 v14, v10
	v_cvt_f32_f16_sdwa v15, v10 dst_sel:DWORD dst_unused:UNUSED_PAD src0_sel:WORD_1
	v_cvt_f32_f16_e32 v10, v11
	v_cvt_f32_f16_sdwa v11, v11 dst_sel:DWORD dst_unused:UNUSED_PAD src0_sel:WORD_1
	v_pk_mul_f32 v[14:15], v[14:15], v[154:155] op_sel_hi:[1,0]
	s_nop 0
	v_med3_f32 v15, v15, s51, v164
	v_pk_mul_f32 v[10:11], v[10:11], v[154:155] op_sel_hi:[1,0]
	v_med3_f32 v14, v14, s51, v164
	v_med3_f32 v10, v10, s51, v164
	v_med3_f32 v11, v11, s51, v164
	v_rndne_f32_e32 v15, v15
	v_rndne_f32_e32 v14, v14
	v_cvt_i32_f32_e32 v15, v15
	v_rndne_f32_e32 v10, v10
	v_rndne_f32_e32 v11, v11
	v_cvt_i32_f32_e32 v14, v14
	v_cvt_i32_f32_sdwa v10, v10 dst_sel:WORD_1 dst_unused:UNUSED_PAD src0_sel:DWORD
	v_cvt_i32_f32_e32 v11, v11
	v_lshlrev_b32_e32 v15, 8, v15
	v_and_b32_e32 v15, 0xff00, v15
	v_and_b32_e32 v10, 0xff0000, v10
	v_perm_b32 v11, v11, v14, s52
	v_or3_b32 v10, v11, v15, v10
	v_cvt_f32_f16_e32 v14, v12
	v_cvt_f32_f16_e32 v15, v170
	v_cvt_f32_f16_e32 v12, v13
	v_cvt_f32_f16_sdwa v13, v13 dst_sel:DWORD dst_unused:UNUSED_PAD src0_sel:WORD_1
	v_pk_mul_f32 v[14:15], v[14:15], v[154:155] op_sel_hi:[1,0]
	s_nop 0
	v_med3_f32 v11, v14, s51, v164
	v_pk_mul_f32 v[12:13], v[12:13], v[154:155] op_sel_hi:[1,0]
	v_med3_f32 v14, v15, s51, v164
	v_med3_f32 v12, v12, s51, v164
	v_med3_f32 v13, v13, s51, v164
	v_rndne_f32_e32 v14, v14
	v_rndne_f32_e32 v11, v11
	v_cvt_i32_f32_e32 v14, v14
	v_rndne_f32_e32 v12, v12
	v_rndne_f32_e32 v13, v13
	v_cvt_i32_f32_e32 v11, v11
	v_cvt_i32_f32_sdwa v12, v12 dst_sel:WORD_1 dst_unused:UNUSED_PAD src0_sel:DWORD
	v_cvt_i32_f32_e32 v13, v13
	v_lshlrev_b32_e32 v14, 8, v14
	v_and_b32_e32 v14, 0xff00, v14
	v_and_b32_e32 v12, 0xff0000, v12
	v_perm_b32 v11, v13, v11, s52
	v_or3_b32 v11, v11, v14, v12
	global_store_dwordx2 v165, v[10:11], s[12:13] offset:512 nt
	v_cvt_f32_f16_e32 v10, v6
	v_cvt_f32_f16_sdwa v11, v6 dst_sel:DWORD dst_unused:UNUSED_PAD src0_sel:WORD_1
	v_cvt_f32_f16_e32 v6, v7
	v_cvt_f32_f16_sdwa v7, v7 dst_sel:DWORD dst_unused:UNUSED_PAD src0_sel:WORD_1
	v_pk_mul_f32 v[10:11], v[10:11], v[154:155] op_sel_hi:[1,0]
	s_nop 0
	v_med3_f32 v11, v11, s51, v164
	v_pk_mul_f32 v[6:7], v[6:7], v[154:155] op_sel_hi:[1,0]
	v_med3_f32 v10, v10, s51, v164
	v_med3_f32 v6, v6, s51, v164
	v_med3_f32 v7, v7, s51, v164
	v_rndne_f32_e32 v11, v11
	v_rndne_f32_e32 v10, v10
	v_cvt_i32_f32_e32 v11, v11
	v_rndne_f32_e32 v6, v6
	v_rndne_f32_e32 v7, v7
	v_cvt_i32_f32_e32 v10, v10
	v_cvt_i32_f32_sdwa v6, v6 dst_sel:WORD_1 dst_unused:UNUSED_PAD src0_sel:DWORD
	v_cvt_i32_f32_e32 v7, v7
	v_lshlrev_b32_e32 v11, 8, v11
	v_and_b32_e32 v11, 0xff00, v11
	v_and_b32_e32 v6, 0xff0000, v6
	v_perm_b32 v7, v7, v10, s52
	v_or3_b32 v6, v7, v11, v6
	v_cvt_f32_f16_e32 v10, v8
	v_cvt_f32_f16_e32 v11, v171
	v_cvt_f32_f16_e32 v8, v9
	v_cvt_f32_f16_sdwa v9, v9 dst_sel:DWORD dst_unused:UNUSED_PAD src0_sel:WORD_1
	v_pk_mul_f32 v[10:11], v[10:11], v[154:155] op_sel_hi:[1,0]
	s_nop 0
	v_med3_f32 v7, v10, s51, v164
	v_pk_mul_f32 v[8:9], v[8:9], v[154:155] op_sel_hi:[1,0]
	v_med3_f32 v10, v11, s51, v164
	v_med3_f32 v8, v8, s51, v164
	v_med3_f32 v9, v9, s51, v164
	v_rndne_f32_e32 v10, v10
	v_rndne_f32_e32 v7, v7
	v_cvt_i32_f32_e32 v10, v10
	v_rndne_f32_e32 v8, v8
	v_rndne_f32_e32 v9, v9
	v_cvt_i32_f32_e32 v7, v7
	v_cvt_i32_f32_sdwa v8, v8 dst_sel:WORD_1 dst_unused:UNUSED_PAD src0_sel:DWORD
	v_cvt_i32_f32_e32 v9, v9
	v_lshlrev_b32_e32 v10, 8, v10
	v_and_b32_e32 v10, 0xff00, v10
	v_and_b32_e32 v8, 0xff0000, v8
	v_perm_b32 v7, v9, v7, s52
	v_or3_b32 v7, v7, v10, v8
	global_store_dwordx2 v165, v[6:7], s[12:13] offset:1024 nt
	v_cvt_f32_f16_e32 v6, v2
	v_cvt_f32_f16_sdwa v7, v2 dst_sel:DWORD dst_unused:UNUSED_PAD src0_sel:WORD_1
	v_cvt_f32_f16_e32 v2, v3
	v_cvt_f32_f16_sdwa v3, v3 dst_sel:DWORD dst_unused:UNUSED_PAD src0_sel:WORD_1
	v_pk_mul_f32 v[6:7], v[6:7], v[154:155] op_sel_hi:[1,0]
	s_nop 0
	v_med3_f32 v7, v7, s51, v164
	v_pk_mul_f32 v[2:3], v[2:3], v[154:155] op_sel_hi:[1,0]
	v_med3_f32 v6, v6, s51, v164
	v_med3_f32 v2, v2, s51, v164
	v_med3_f32 v3, v3, s51, v164
	v_rndne_f32_e32 v7, v7
	v_rndne_f32_e32 v6, v6
	v_cvt_i32_f32_e32 v7, v7
	v_rndne_f32_e32 v2, v2
	v_rndne_f32_e32 v3, v3
	v_cvt_i32_f32_e32 v6, v6
	v_cvt_i32_f32_sdwa v2, v2 dst_sel:WORD_1 dst_unused:UNUSED_PAD src0_sel:DWORD
	v_cvt_i32_f32_e32 v3, v3
	v_lshlrev_b32_e32 v7, 8, v7
	v_and_b32_e32 v7, 0xff00, v7
	v_and_b32_e32 v2, 0xff0000, v2
	v_perm_b32 v3, v3, v6, s52
	v_or3_b32 v2, v3, v7, v2
	v_cvt_f32_f16_e32 v6, v4
	v_cvt_f32_f16_e32 v7, v172
	v_cvt_f32_f16_e32 v4, v5
	v_cvt_f32_f16_sdwa v5, v5 dst_sel:DWORD dst_unused:UNUSED_PAD src0_sel:WORD_1
	v_pk_mul_f32 v[6:7], v[6:7], v[154:155] op_sel_hi:[1,0]
	s_nop 0
	v_med3_f32 v3, v6, s51, v164
	v_pk_mul_f32 v[4:5], v[4:5], v[154:155] op_sel_hi:[1,0]
	v_med3_f32 v6, v7, s51, v164
	v_med3_f32 v4, v4, s51, v164
	v_med3_f32 v5, v5, s51, v164
	v_rndne_f32_e32 v6, v6
	v_rndne_f32_e32 v3, v3
	v_cvt_i32_f32_e32 v6, v6
	v_rndne_f32_e32 v4, v4
	v_rndne_f32_e32 v5, v5
	v_cvt_i32_f32_e32 v3, v3
	v_cvt_i32_f32_sdwa v4, v4 dst_sel:WORD_1 dst_unused:UNUSED_PAD src0_sel:DWORD
	v_cvt_i32_f32_e32 v5, v5
	v_lshlrev_b32_e32 v6, 8, v6
	v_and_b32_e32 v6, 0xff00, v6
	v_and_b32_e32 v4, 0xff0000, v4
	v_perm_b32 v3, v5, v3, s52
	v_or3_b32 v3, v3, v6, v4
	global_store_dwordx2 v165, v[2:3], s[12:13] offset:1536 nt
	s_and_saveexec_b64 s[12:13], s[4:5]
	s_cbranch_execz .LBB0_17
	s_lshl_b32 s16, s14, 2
	v_mov_b32_e32 v2, s16
	global_store_dword v2, v166, s[28:29] offset:12
	s_branch .LBB0_17
	s_nop 0
	s_nop 0
	s_nop 0
	s_nop 0
	s_nop 0
	s_nop 0
	s_nop 0
	s_nop 0
	s_nop 0
	s_nop 0
	s_nop 0
	s_nop 0
